# attention: softmax row-sum kept as per-lane partials in the loop, halves combined once at loop exit (no per-step permlane/mov)
# baseline (speedup 1.0000x reference)
; DI void finishSM(f32x16& p0, f32x16& p1, float alpha, float& l_reg, bf16x8& pa0, bf16x8& pa1, bf16x8& pa2, bf16x8& pa3) {
; #pragma unroll
;     for (int r = 0; r < 16; ++r) p1[r] = __builtin_amdgcn_exp2f(p1[r]);
;     float ps = 0;
; #pragma unroll
;     for (int r = 0; r < 16; ++r) ps += p0[r];
; #pragma unroll
;     for (int r = 0; r < 16; ++r) ps += p1[r];
;     { auto rr = __builtin_amdgcn_permlane32_swap(__float_as_uint(ps), __float_as_uint(ps), false, false); ps = __uint_as_float(rr[0]) + __uint_as_float(rr[1]); }
;     l_reg = l_reg * alpha + ps;
;     ...
;     AT_PK4(p0, 0, pa0); AT_PK4(p0, 8, pa1); AT_PK4(p1, 0, pa2); AT_PK4(p1, 8, pa3);
;     ...
; }
; DI void qkt(f32x16& p0, f32x16& p1, const char* Ks, const bf16x8* qr, const f32x16& negm, int r32, int hi) {
; #pragma unroll
;     for (int d0 = 0; d0 < 4; ++d0) { const int cb = (d0 * 16 + hi * 8) * 2;
;         const bf16x8 b0 = *reinterpret_cast<const bf16x8*>(Ks + AT_KSWZ(r32, cb));
;         const bf16x8 b1 = *reinterpret_cast<const bf16x8*>(Ks + AT_KSWZ(32 + r32, cb));
;         p0 = __builtin_amdgcn_mfma_f32_32x32x16_bf16(b0, qr[d0], d0 == 0 ? negm : p0, 0, 0, 0);
;         p1 = __builtin_amdgcn_mfma_f32_32x32x16_bf16(b1, qr[d0], d0 == 0 ? negm : p1, 0, 0, 0); }
.LBB4_702:
	s_lshl_b32 s26, s66, 13
	s_add_i32 s26, s26, 0
	v_add_u32_e32 v72, s26, v205
	v_add_u32_e32 v112, s26, v206
	v_add_u32_e32 v180, s26, v207
	s_waitcnt lgkmcnt(1)
	v_mfma_f32_32x32x16_bf16 v[128:143], v[64:67], v[156:159], v[80:95]
	ds_read_b128 v[64:67], v72 offset:49152
	ds_read_b128 v[72:75], v72 offset:53248
	ds_read_b128 v[76:79], v112 offset:49152
	ds_read_b128 v[220:223], v112 offset:53248
	v_exp_f32_e32 v186, v97
	v_exp_f32_e32 v213, v98
	v_exp_f32_e32 v214, v99
	v_exp_f32_e32 v219, v100
	v_exp_f32_e32 v228, v101
	s_waitcnt lgkmcnt(4)
	v_mfma_f32_32x32x16_bf16 v[112:127], v[68:71], v[156:159], v[80:95]
	ds_read_b128 v[68:71], v180 offset:49152
	ds_read_b128 v[224:227], v180 offset:53248
	v_exp_f32_e32 v180, v96
	v_cvt_pk_bf16_f32 v96, v216, v218
	v_cvt_pk_bf16_f32 v97, v179, v217
	v_cvt_pk_bf16_f32 v98, v177, v215
	v_cvt_pk_bf16_f32 v99, v176, v178
	s_waitcnt lgkmcnt(4)
	v_mfma_f32_32x32x16_bf16 v[112:127], v[72:75], v[152:155], v[112:127]
	v_add_f32_e32 v75, 0, v216
	v_add_f32_e32 v75, v218, v75
	v_add_f32_e32 v75, v179, v75
	v_add_f32_e32 v75, v217, v75
	v_add_f32_e32 v75, v177, v75
	v_add_f32_e32 v75, v215, v75
	v_add_f32_e32 v75, v176, v75
	v_mfma_f32_32x32x16_bf16 v[128:143], v[64:67], v[152:155], v[128:143]
	v_add_f32_e32 v75, v178, v75
	v_add_f32_e32 v75, v173, v75
	v_add_f32_e32 v75, v175, v75
	v_add_f32_e32 v75, v171, v75
	v_add_f32_e32 v75, v174, v75
	v_add_f32_e32 v75, v169, v75
	v_add_f32_e32 v75, v172, v75
	s_waitcnt lgkmcnt(3)
	v_mfma_f32_32x32x16_bf16 v[128:143], v[76:79], v[148:151], v[128:143]
	v_add_f32_e32 v75, v168, v75
	v_add_f32_e32 v75, v170, v75
	v_add_f32_e32 v75, v180, v75
	v_add_f32_e32 v75, v186, v75
	v_exp_f32_e32 v64, v102
	v_exp_f32_e32 v65, v103
	v_exp_f32_e32 v66, v104
	s_waitcnt lgkmcnt(2)
	v_mfma_f32_32x32x16_bf16 v[112:127], v[220:223], v[148:151], v[112:127]
	v_exp_f32_e32 v67, v105
	v_exp_f32_e32 v105, v106
	v_exp_f32_e32 v106, v107
	v_exp_f32_e32 v107, v108
	v_exp_f32_e32 v72, v109
	v_exp_f32_e32 v73, v110
	v_exp_f32_e32 v74, v111
	s_waitcnt lgkmcnt(1)
	v_mfma_f32_32x32x16_bf16 v[128:143], v[68:71], v[144:147], v[128:143]
	v_add_f32_e32 v68, v213, v75
	v_add_f32_e32 v68, v214, v68
	v_add_f32_e32 v68, v219, v68
	v_add_f32_e32 v68, v228, v68
	v_add_f32_e32 v68, v64, v68
	v_add_f32_e32 v68, v65, v68
	v_add_f32_e32 v68, v66, v68
	v_add_f32_e32 v68, v67, v68
	s_waitcnt lgkmcnt(0)
	v_mfma_f32_32x32x16_bf16 v[112:127], v[224:227], v[144:147], v[112:127]
	v_add_f32_e32 v68, v105, v68
	v_add_f32_e32 v68, v106, v68
	v_add_f32_e32 v68, v107, v68
	v_add_f32_e32 v68, v72, v68
	v_add_f32_e32 v68, v73, v68
	v_add_f32_e32 v183, v74, v68
	v_cvt_pk_bf16_f32 v108, v173, v175
	v_cvt_pk_bf16_f32 v109, v171, v174
	v_cvt_pk_bf16_f32 v110, v169, v172
	v_cvt_pk_bf16_f32 v111, v168, v170
	v_cvt_pk_bf16_f32 v100, v180, v186
	v_cvt_pk_bf16_f32 v101, v213, v214
	v_cvt_pk_bf16_f32 v102, v219, v228
	v_cvt_pk_bf16_f32 v103, v64, v65
	v_cvt_pk_bf16_f32 v104, v66, v67
	v_cvt_pk_bf16_f32 v105, v105, v106
	v_cvt_pk_bf16_f32 v106, v107, v72
	v_cvt_pk_bf16_f32 v107, v73, v74
	s_add_u32 s74, s46, s28
	s_addc_u32 s75, s47, s29
	s_add_u32 s78, s74, 0x23808000
	s_addc_u32 s79, s75, 0
	s_add_u32 s80, s74, 0x2380a000
	s_addc_u32 s81, s75, 0
	s_add_u32 s76, s46, s30
	s_addc_u32 s77, s47, s31
	s_add_u32 s82, s76, 0x21804000
	s_addc_u32 s83, s77, 0
	global_load_dwordx4 v[176:179], v197, s[78:79]
	global_load_dwordx4 v[172:175], v197, s[80:81]
	global_load_dwordx4 v[168:171], v198, s[82:83]
	s_andn2_b64 vcc, exec, s[2:3]
	s_cbranch_vccnz .LBB4_704
	s_mov_b64 s[2:3], s[8:9]
	global_store_dwordx2 v189, v[184:185], s[2:3] nt

; DI void finishSM(f32x16& p0, f32x16& p1, float alpha, float& l_reg, bf16x8& pa0, bf16x8& pa1, bf16x8& pa2, bf16x8& pa3) {
; #pragma unroll
;     for (int r = 0; r < 16; ++r) p1[r] = __builtin_amdgcn_exp2f(p1[r]);
;     float ps = 0;
; #pragma unroll
;     for (int r = 0; r < 16; ++r) ps += p0[r];
; #pragma unroll
;     for (int r = 0; r < 16; ++r) ps += p1[r];
;     { auto rr = __builtin_amdgcn_permlane32_swap(__float_as_uint(ps), __float_as_uint(ps), false, false); ps = __uint_as_float(rr[0]) + __uint_as_float(rr[1]); }
;     l_reg = l_reg * alpha + ps;
;     ...
;     AT_PK4(p0, 0, pa0); AT_PK4(p0, 8, pa1); AT_PK4(p1, 0, pa2); AT_PK4(p1, 8, pa3);
;     ...
; }
; DI void qkt(f32x16& p0, f32x16& p1, const char* Ks, const bf16x8* qr, const f32x16& negm, int r32, int hi) {
; #pragma unroll
;     for (int d0 = 0; d0 < 4; ++d0) { const int cb = (d0 * 16 + hi * 8) * 2;
;         const bf16x8 b0 = *reinterpret_cast<const bf16x8*>(Ks + AT_KSWZ(r32, cb));
;         const bf16x8 b1 = *reinterpret_cast<const bf16x8*>(Ks + AT_KSWZ(32 + r32, cb));
;         p0 = __builtin_amdgcn_mfma_f32_32x32x16_bf16(b0, qr[d0], d0 == 0 ? negm : p0, 0, 0, 0);
;         p1 = __builtin_amdgcn_mfma_f32_32x32x16_bf16(b1, qr[d0], d0 == 0 ? negm : p1, 0, 0, 0); }
.LBB4_723:
	v_exp_f32_e32 v186, v128
	v_exp_f32_e32 v230, v129
	v_exp_f32_e32 v231, v130
	v_exp_f32_e32 v232, v131
	v_exp_f32_e32 v233, v132
	v_exp_f32_e32 v234, v133
	v_exp_f32_e32 v235, v134
	v_exp_f32_e32 v236, v135
	v_exp_f32_e32 v237, v136
	v_exp_f32_e32 v238, v137
	v_exp_f32_e32 v239, v138
	v_exp_f32_e32 v240, v139
	v_exp_f32_e32 v241, v140
	v_exp_f32_e32 v242, v141
	v_exp_f32_e32 v243, v142
	v_exp_f32_e32 v244, v143
	v_add_u32_e32 v101, s78, v205
	v_add_u32_e32 v102, s78, v206
	v_add_u32_e32 v103, s78, v207
	ds_read_b128 v[172:175], v101 offset:49152
	ds_read_b128 v[176:179], v101 offset:53248
	ds_read_b128 v[214:217], v102 offset:49152
	ds_read_b128 v[218:221], v102 offset:53248
	ds_read_b128 v[222:225], v103 offset:49152
	ds_read_b128 v[226:229], v103 offset:53248
	v_exp_f32_e32 v112, v112
	v_exp_f32_e32 v113, v113
	v_exp_f32_e32 v114, v114
	s_waitcnt lgkmcnt(7)
	v_mfma_f32_32x32x16_bf16 v[128:143], v[96:99], v[156:159], v[80:95]
	v_exp_f32_e32 v115, v115
	v_exp_f32_e32 v116, v116
	v_exp_f32_e32 v117, v117
	v_exp_f32_e32 v118, v118
	v_exp_f32_e32 v119, v119
	s_waitcnt lgkmcnt(6)
	v_mfma_f32_32x32x16_bf16 v[96:111], v[168:171], v[156:159], v[80:95]
	v_exp_f32_e32 v168, v120
	v_add_f32_e32 v120, 0, v186
	v_add_f32_e32 v120, v230, v120
	v_add_f32_e32 v120, v231, v120
	v_add_f32_e32 v120, v232, v120
	v_add_f32_e32 v120, v233, v120
	v_add_f32_e32 v120, v234, v120
	v_add_f32_e32 v120, v235, v120
	v_add_f32_e32 v120, v236, v120
	v_add_f32_e32 v120, v237, v120
	v_add_f32_e32 v120, v238, v120
	s_waitcnt lgkmcnt(5)
	v_mfma_f32_32x32x16_bf16 v[128:143], v[172:175], v[152:155], v[128:143]
	v_add_f32_e32 v120, v239, v120
	v_add_f32_e32 v120, v240, v120
	v_add_f32_e32 v120, v241, v120
	v_add_f32_e32 v120, v242, v120
	v_add_f32_e32 v120, v243, v120
	v_add_f32_e32 v120, v244, v120
	v_add_f32_e32 v120, v112, v120
	s_waitcnt lgkmcnt(4)
	v_mfma_f32_32x32x16_bf16 v[96:111], v[176:179], v[152:155], v[96:111]
	v_add_f32_e32 v120, v113, v120
	v_add_f32_e32 v120, v114, v120
	v_add_f32_e32 v120, v115, v120
	v_add_f32_e32 v120, v116, v120
	v_exp_f32_e32 v169, v121
	v_add_f32_e32 v120, v117, v120
	v_exp_f32_e32 v170, v122
	s_waitcnt lgkmcnt(3)
	v_mfma_f32_32x32x16_bf16 v[128:143], v[214:217], v[148:151], v[128:143]
	v_add_f32_e32 v120, v118, v120
	v_exp_f32_e32 v171, v123
	v_add_f32_e32 v120, v119, v120
	v_exp_f32_e32 v172, v124
	v_add_f32_e32 v120, v168, v120
	v_exp_f32_e32 v173, v125
	v_add_f32_e32 v120, v169, v120
	s_waitcnt lgkmcnt(2)
	v_mfma_f32_32x32x16_bf16 v[96:111], v[218:221], v[148:151], v[96:111]
	v_exp_f32_e32 v174, v126
	v_add_f32_e32 v120, v170, v120
	v_exp_f32_e32 v175, v127
	v_add_f32_e32 v120, v171, v120
	v_add_f32_e32 v120, v172, v120
	v_add_f32_e32 v120, v173, v120
	v_add_f32_e32 v120, v174, v120
	s_waitcnt lgkmcnt(1)
	v_mfma_f32_32x32x16_bf16 v[128:143], v[222:225], v[144:147], v[128:143]
	v_add_f32_e32 v213, v175, v120
	v_cvt_pk_bf16_f32 v120, v186, v230
	v_cvt_pk_bf16_f32 v121, v231, v232
	v_cvt_pk_bf16_f32 v122, v233, v234
	v_cvt_pk_bf16_f32 v123, v235, v236
	v_cvt_pk_bf16_f32 v124, v237, v238
	s_waitcnt lgkmcnt(0)
	v_mfma_f32_32x32x16_bf16 v[96:111], v[226:229], v[144:147], v[96:111]
	v_cvt_pk_bf16_f32 v125, v239, v240
	v_cvt_pk_bf16_f32 v126, v241, v242
	v_cvt_pk_bf16_f32 v127, v243, v244
	v_cvt_pk_bf16_f32 v112, v112, v113
	v_cvt_pk_bf16_f32 v113, v114, v115
	v_cvt_pk_bf16_f32 v114, v116, v117
	v_cvt_pk_bf16_f32 v115, v118, v119
	v_cvt_pk_bf16_f32 v116, v168, v169
	v_cvt_pk_bf16_f32 v117, v170, v171
	v_cvt_pk_bf16_f32 v118, v172, v173
	v_cvt_pk_bf16_f32 v119, v174, v175
	s_add_u32 s78, s74, 0x2380c000
	s_addc_u32 s79, s75, 0
	s_add_u32 s74, s74, 0x2380e000
	s_addc_u32 s75, s75, 0
	s_add_u32 s76, s76, 0x21806000
	s_addc_u32 s77, s77, 0
	global_load_dwordx4 v[176:179], v197, s[78:79]
	global_load_dwordx4 v[172:175], v197, s[74:75]
	s_nop 0
	global_load_dwordx4 v[168:171], v198, s[76:77]
	s_and_b64 vcc, exec, s[2:3]
	s_cbranch_vccnz .LBB4_725
	s_mov_b64 s[2:3], s[8:9]
	global_store_dwordx2 v189, v[184:185], s[2:3] nt

; DI void pv_all_sm(f32x16* o, int vb, bf16x8 pa0, bf16x8 pa1, bf16x8 pa2, bf16x8 pa3, f32x16& p0, f32x16& p1, float& m_ref, f32x16& negm, float& alpha) {
;     ...
;     pv_one<3>(o[3], vb, pa0, pa1, pa2, pa3);
; #pragma unroll
;     for (int r = 0; r < 16; ++r) p0[r] = __builtin_amdgcn_exp2f(p0[r]);
; DI void attn_pass(const Frame& F, CvRide& cv, const bf16_t* __restrict__ Qb, const bf16_t* __restrict__ Kh, const bf16_t* __restrict__ Vh, char* lds, f32x16 (&o)[4], float& l_out, const int wave_s) {
;     ...
;     for (int j = 1; j + 2 < NT; j += 2) {
;         AT_STEP(pB0, pB1, pA0, pA1, alB, alA, j, true);
;         AT_STEP(pA0, pA1, pB0, pB1, alA, alB, j + 1, true);
;     }
.LBB4_733:
	s_add_u32 s30, s30, 0x4000
	v_exp_f32_e32 v216, v128
	v_exp_f32_e32 v218, v129
	v_exp_f32_e32 v179, v130
	v_exp_f32_e32 v217, v131
	v_exp_f32_e32 v177, v132
	v_exp_f32_e32 v215, v133
	v_exp_f32_e32 v176, v134
	v_exp_f32_e32 v178, v135
	v_exp_f32_e32 v173, v136
	v_exp_f32_e32 v175, v137
	v_exp_f32_e32 v171, v138
	v_exp_f32_e32 v174, v139
	v_exp_f32_e32 v169, v140
	v_exp_f32_e32 v172, v141
	v_exp_f32_e32 v168, v142
	v_exp_f32_e32 v170, v143
	s_addc_u32 s31, s31, 0
	s_add_u32 s28, s28, 0x8000
	v_fma_f32 v112, v210, v182, v183
	s_addc_u32 s29, s29, 0
	s_add_i32 s15, s15, 2
	v_fma_f32 v182, v112, v180, v213
	s_cmp_gt_u32 s15, 61
	s_waitcnt lgkmcnt(0)
	s_barrier
	s_cbranch_scc1 .LBB4_739
	s_mov_b32 s34, s64
	s_mov_b32 s64, s66
	v_mov_b32_e32 v210, v186
	s_branch .LBB4_692

; #define AT_SBAR() __builtin_amdgcn_sched_barrier(0)
; #define AT_CV_READ() do { if (cv.pend) { const char* t_ = lds + cv_lr + ((cv.ci - 1) & 1) * CV_TILE; cvr0 = *(const unsigned*)t_; cvr1 = *(const unsigned*)(t_ + 4); } } while (0)
; #define AT_CV_STORE() do { if (cv.pend) { GAS unsigned char* gd_ = (GAS unsigned char*)cv.sdst; unsigned o_ = cv_sto; asm volatile("" : "+s"(gd_), "+v"(o_)); __builtin_nontemporal_store((u32x2){cvr0, cvr1}, (GAS u32x2*)(gd_ + (size_t)o_)); cv.pend = 0; } } while (0)
; DI void attn_pass(const Frame& F, CvRide& cv, const bf16_t* __restrict__ Qb, const bf16_t* __restrict__ Kh, const bf16_t* __restrict__ Vh, char* lds, f32x16 (&o)[4], float& l_out, const int wave_s) {
;     ...
;     AT_STEP(pB0, pB1, pA0, pA1, alB, alA, NT - 1, false);
;     AT_CV_READ(); AT_CV_STORE();
;     finishSM(pB0, pB1, alB, l_reg, pa0, pa1, pa2, pa3); AT_SBAR();
.LBB4_739:
	v_mov_b32_e32 v254, v182
	s_nop 1
	v_permlane32_swap_b32_e32 v182, v254
	v_add_f32_e32 v182, v182, v254
	v_mov_b64_e32 v[64:65], v[80:81]
	v_mov_b64_e32 v[66:67], v[82:83]
	v_mov_b64_e32 v[68:69], v[84:85]
	v_mov_b64_e32 v[70:71], v[86:87]
	v_mov_b64_e32 v[72:73], v[88:89]
	v_mov_b64_e32 v[74:75], v[90:91]
	v_mov_b64_e32 v[76:77], v[92:93]
	v_mov_b64_e32 v[78:79], v[94:95]
	s_and_b64 vcc, exec, s[34:35]
	s_cbranch_vccz .LBB4_741
	s_andn2_b32 s15, 1, s58
	s_mulk_i32 s15, 0x1100
	v_add_u32_e32 v80, s15, v190
	ds_read2_b32 v[184:185], v80 offset1:1

; DI void finishSM(f32x16& p0, f32x16& p1, float alpha, float& l_reg, bf16x8& pa0, bf16x8& pa1, bf16x8& pa2, bf16x8& pa3) {
; #pragma unroll
;     for (int r = 0; r < 16; ++r) p1[r] = __builtin_amdgcn_exp2f(p1[r]);
;     float ps = 0;
; #pragma unroll
;     for (int r = 0; r < 16; ++r) ps += p0[r];
; #pragma unroll
;     for (int r = 0; r < 16; ++r) ps += p1[r];
;     { auto rr = __builtin_amdgcn_permlane32_swap(__float_as_uint(ps), __float_as_uint(ps), false, false); ps = __uint_as_float(rr[0]) + __uint_as_float(rr[1]); }
;     l_reg = l_reg * alpha + ps;
;     ...
;     AT_PK4(p0, 0, pa0); AT_PK4(p0, 8, pa1); AT_PK4(p1, 0, pa2); AT_PK4(p1, 8, pa3);
;     ...
; }
; DI void qkt(f32x16& p0, f32x16& p1, const char* Ks, const bf16x8* qr, const f32x16& negm, int r32, int hi) {
; #pragma unroll
;     for (int d0 = 0; d0 < 4; ++d0) { const int cb = (d0 * 16 + hi * 8) * 2;
;         const bf16x8 b0 = *reinterpret_cast<const bf16x8*>(Ks + AT_KSWZ(r32, cb));
;         const bf16x8 b1 = *reinterpret_cast<const bf16x8*>(Ks + AT_KSWZ(32 + r32, cb));
;         p0 = __builtin_amdgcn_mfma_f32_32x32x16_bf16(b0, qr[d0], d0 == 0 ? negm : p0, 0, 0, 0);
;         p1 = __builtin_amdgcn_mfma_f32_32x32x16_bf16(b1, qr[d0], d0 == 0 ? negm : p1, 0, 0, 0); }
.LBB4_775:
	s_lshl_b32 s20, s30, 13
	s_add_i32 s20, s20, 0
	v_add_u32_e32 v72, s20, v208
	v_add_u32_e32 v112, s20, v209
	v_add_u32_e32 v180, s20, v210
	s_waitcnt lgkmcnt(1)
	v_mfma_f32_32x32x16_bf16 v[128:143], v[64:67], v[156:159], v[80:95]
	ds_read_b128 v[64:67], v72 offset:49152
	ds_read_b128 v[72:75], v72 offset:53248
	ds_read_b128 v[76:79], v112 offset:49152
	ds_read_b128 v[224:227], v112 offset:53248
	v_exp_f32_e32 v182, v97
	v_exp_f32_e32 v217, v98
	v_exp_f32_e32 v218, v99
	v_exp_f32_e32 v223, v100
	v_exp_f32_e32 v232, v101
	s_waitcnt lgkmcnt(4)
	v_mfma_f32_32x32x16_bf16 v[112:127], v[68:71], v[156:159], v[80:95]
	ds_read_b128 v[68:71], v180 offset:49152
	ds_read_b128 v[228:231], v180 offset:53248
	v_exp_f32_e32 v180, v96
	v_cvt_pk_bf16_f32 v96, v220, v222
	v_cvt_pk_bf16_f32 v97, v179, v221
	v_cvt_pk_bf16_f32 v98, v177, v219
	v_cvt_pk_bf16_f32 v99, v176, v178
	s_waitcnt lgkmcnt(4)
	v_mfma_f32_32x32x16_bf16 v[112:127], v[72:75], v[152:155], v[112:127]
	v_add_f32_e32 v75, 0, v220
	v_add_f32_e32 v75, v222, v75
	v_add_f32_e32 v75, v179, v75
	v_add_f32_e32 v75, v221, v75
	v_add_f32_e32 v75, v177, v75
	v_add_f32_e32 v75, v219, v75
	v_add_f32_e32 v75, v176, v75
	v_mfma_f32_32x32x16_bf16 v[128:143], v[64:67], v[152:155], v[128:143]
	v_add_f32_e32 v75, v178, v75
	v_add_f32_e32 v75, v173, v75
	v_add_f32_e32 v75, v175, v75
	v_add_f32_e32 v75, v171, v75
	v_add_f32_e32 v75, v174, v75
	v_add_f32_e32 v75, v169, v75
	v_add_f32_e32 v75, v172, v75
	s_waitcnt lgkmcnt(3)
	v_mfma_f32_32x32x16_bf16 v[128:143], v[76:79], v[148:151], v[128:143]
	v_add_f32_e32 v75, v168, v75
	v_add_f32_e32 v75, v170, v75
	v_add_f32_e32 v75, v180, v75
	v_add_f32_e32 v75, v182, v75
	v_exp_f32_e32 v64, v102
	v_exp_f32_e32 v65, v103
	v_exp_f32_e32 v66, v104
	s_waitcnt lgkmcnt(2)
	v_mfma_f32_32x32x16_bf16 v[112:127], v[224:227], v[148:151], v[112:127]
	v_exp_f32_e32 v67, v105
	v_exp_f32_e32 v105, v106
	v_exp_f32_e32 v106, v107
	v_exp_f32_e32 v107, v108
	v_exp_f32_e32 v72, v109
	v_exp_f32_e32 v73, v110
	v_exp_f32_e32 v74, v111
	s_waitcnt lgkmcnt(1)
	v_mfma_f32_32x32x16_bf16 v[128:143], v[68:71], v[144:147], v[128:143]
	v_add_f32_e32 v68, v217, v75
	v_add_f32_e32 v68, v218, v68
	v_add_f32_e32 v68, v223, v68
	v_add_f32_e32 v68, v232, v68
	v_add_f32_e32 v68, v64, v68
	v_add_f32_e32 v68, v65, v68
	v_add_f32_e32 v68, v66, v68
	v_add_f32_e32 v68, v67, v68
	s_waitcnt lgkmcnt(0)
	v_mfma_f32_32x32x16_bf16 v[112:127], v[228:231], v[144:147], v[112:127]
	v_add_f32_e32 v68, v105, v68
	v_add_f32_e32 v68, v106, v68
	v_add_f32_e32 v68, v107, v68
	v_add_f32_e32 v68, v72, v68
	v_add_f32_e32 v68, v73, v68
	v_add_f32_e32 v215, v74, v68
	v_cvt_pk_bf16_f32 v108, v173, v175
	v_cvt_pk_bf16_f32 v109, v171, v174
	v_cvt_pk_bf16_f32 v110, v169, v172
	v_cvt_pk_bf16_f32 v111, v168, v170
	v_cvt_pk_bf16_f32 v100, v180, v182
	v_cvt_pk_bf16_f32 v101, v217, v218
	v_cvt_pk_bf16_f32 v102, v223, v232
	v_cvt_pk_bf16_f32 v103, v64, v65
	v_cvt_pk_bf16_f32 v104, v66, v67
	v_cvt_pk_bf16_f32 v105, v105, v106
	v_cvt_pk_bf16_f32 v106, v107, v72
	v_cvt_pk_bf16_f32 v107, v73, v74
	s_add_u32 s34, s46, s16
	s_addc_u32 s35, s47, s17
	s_add_u32 s24, s34, 0x23808000
	s_addc_u32 s25, s35, 0
	s_add_u32 s66, s34, 0x2380a000
	s_addc_u32 s67, s35, 0
	s_add_u32 s37, s46, s18
	s_addc_u32 s64, s47, s19
	s_add_u32 s74, s37, 0x21884000
	s_addc_u32 s75, s64, 0
	global_load_dwordx4 v[176:179], v200, s[24:25]
	global_load_dwordx4 v[172:175], v200, s[66:67]
	global_load_dwordx4 v[168:171], v201, s[74:75]
	s_andn2_b64 vcc, exec, s[2:3]
	s_cbranch_vccnz .LBB4_777
	s_mov_b64 s[2:3], s[8:9]
	global_store_dwordx2 v193, v[184:185], s[2:3] nt

; DI void finishSM(f32x16& p0, f32x16& p1, float alpha, float& l_reg, bf16x8& pa0, bf16x8& pa1, bf16x8& pa2, bf16x8& pa3) {
; #pragma unroll
;     for (int r = 0; r < 16; ++r) p1[r] = __builtin_amdgcn_exp2f(p1[r]);
;     float ps = 0;
; #pragma unroll
;     for (int r = 0; r < 16; ++r) ps += p0[r];
; #pragma unroll
;     for (int r = 0; r < 16; ++r) ps += p1[r];
;     { auto rr = __builtin_amdgcn_permlane32_swap(__float_as_uint(ps), __float_as_uint(ps), false, false); ps = __uint_as_float(rr[0]) + __uint_as_float(rr[1]); }
;     l_reg = l_reg * alpha + ps;
;     ...
;     AT_PK4(p0, 0, pa0); AT_PK4(p0, 8, pa1); AT_PK4(p1, 0, pa2); AT_PK4(p1, 8, pa3);
;     ...
; }
; DI void qkt(f32x16& p0, f32x16& p1, const char* Ks, const bf16x8* qr, const f32x16& negm, int r32, int hi) {
; #pragma unroll
;     for (int d0 = 0; d0 < 4; ++d0) { const int cb = (d0 * 16 + hi * 8) * 2;
;         const bf16x8 b0 = *reinterpret_cast<const bf16x8*>(Ks + AT_KSWZ(r32, cb));
;         const bf16x8 b1 = *reinterpret_cast<const bf16x8*>(Ks + AT_KSWZ(32 + r32, cb));
;         p0 = __builtin_amdgcn_mfma_f32_32x32x16_bf16(b0, qr[d0], d0 == 0 ? negm : p0, 0, 0, 0);
;         p1 = __builtin_amdgcn_mfma_f32_32x32x16_bf16(b1, qr[d0], d0 == 0 ? negm : p1, 0, 0, 0); }
.LBB4_796:
	v_exp_f32_e32 v182, v128
	v_exp_f32_e32 v234, v129
	v_exp_f32_e32 v235, v130
	v_exp_f32_e32 v236, v131
	v_exp_f32_e32 v237, v132
	v_exp_f32_e32 v238, v133
	v_exp_f32_e32 v239, v134
	v_exp_f32_e32 v240, v135
	v_exp_f32_e32 v241, v136
	v_exp_f32_e32 v242, v137
	v_exp_f32_e32 v243, v138
	v_exp_f32_e32 v244, v139
	v_exp_f32_e32 v245, v140
	v_exp_f32_e32 v246, v141
	v_exp_f32_e32 v247, v142
	v_exp_f32_e32 v248, v143
	v_add_u32_e32 v101, s65, v208
	v_add_u32_e32 v102, s65, v209
	v_add_u32_e32 v103, s65, v210
	ds_read_b128 v[172:175], v101 offset:49152
	ds_read_b128 v[176:179], v101 offset:53248
	ds_read_b128 v[218:221], v102 offset:49152
	ds_read_b128 v[222:225], v102 offset:53248
	ds_read_b128 v[226:229], v103 offset:49152
	ds_read_b128 v[230:233], v103 offset:53248
	v_exp_f32_e32 v112, v112
	v_exp_f32_e32 v113, v113
	v_exp_f32_e32 v114, v114
	s_waitcnt lgkmcnt(7)
	v_mfma_f32_32x32x16_bf16 v[128:143], v[96:99], v[156:159], v[80:95]
	v_exp_f32_e32 v115, v115
	v_exp_f32_e32 v116, v116
	v_exp_f32_e32 v117, v117
	v_exp_f32_e32 v118, v118
	v_exp_f32_e32 v119, v119
	s_waitcnt lgkmcnt(6)
	v_mfma_f32_32x32x16_bf16 v[96:111], v[168:171], v[156:159], v[80:95]
	v_exp_f32_e32 v168, v120
	v_add_f32_e32 v120, 0, v182
	v_add_f32_e32 v120, v234, v120
	v_add_f32_e32 v120, v235, v120
	v_add_f32_e32 v120, v236, v120
	v_add_f32_e32 v120, v237, v120
	v_add_f32_e32 v120, v238, v120
	v_add_f32_e32 v120, v239, v120
	v_add_f32_e32 v120, v240, v120
	v_add_f32_e32 v120, v241, v120
	v_add_f32_e32 v120, v242, v120
	s_waitcnt lgkmcnt(5)
	v_mfma_f32_32x32x16_bf16 v[128:143], v[172:175], v[152:155], v[128:143]
	v_add_f32_e32 v120, v243, v120
	v_add_f32_e32 v120, v244, v120
	v_add_f32_e32 v120, v245, v120
	v_add_f32_e32 v120, v246, v120
	v_add_f32_e32 v120, v247, v120
	v_add_f32_e32 v120, v248, v120
	v_add_f32_e32 v120, v112, v120
	s_waitcnt lgkmcnt(4)
	v_mfma_f32_32x32x16_bf16 v[96:111], v[176:179], v[152:155], v[96:111]
	v_add_f32_e32 v120, v113, v120
	v_add_f32_e32 v120, v114, v120
	v_add_f32_e32 v120, v115, v120
	v_add_f32_e32 v120, v116, v120
	v_exp_f32_e32 v169, v121
	v_add_f32_e32 v120, v117, v120
	v_exp_f32_e32 v170, v122
	s_waitcnt lgkmcnt(3)
	v_mfma_f32_32x32x16_bf16 v[128:143], v[218:221], v[148:151], v[128:143]
	v_add_f32_e32 v120, v118, v120
	v_exp_f32_e32 v171, v123
	v_add_f32_e32 v120, v119, v120
	v_exp_f32_e32 v172, v124
	v_add_f32_e32 v120, v168, v120
	v_exp_f32_e32 v173, v125
	v_add_f32_e32 v120, v169, v120
	s_waitcnt lgkmcnt(2)
	v_mfma_f32_32x32x16_bf16 v[96:111], v[222:225], v[148:151], v[96:111]
	v_exp_f32_e32 v174, v126
	v_add_f32_e32 v120, v170, v120
	v_exp_f32_e32 v175, v127
	v_add_f32_e32 v120, v171, v120
	v_add_f32_e32 v120, v172, v120
	v_add_f32_e32 v120, v173, v120
	v_add_f32_e32 v120, v174, v120
	s_waitcnt lgkmcnt(1)
	v_mfma_f32_32x32x16_bf16 v[128:143], v[226:229], v[144:147], v[128:143]
	v_add_f32_e32 v217, v175, v120
	v_cvt_pk_bf16_f32 v120, v182, v234
	v_cvt_pk_bf16_f32 v121, v235, v236
	v_cvt_pk_bf16_f32 v122, v237, v238
	v_cvt_pk_bf16_f32 v123, v239, v240
	v_cvt_pk_bf16_f32 v124, v241, v242
	s_waitcnt lgkmcnt(0)
	v_mfma_f32_32x32x16_bf16 v[96:111], v[230:233], v[144:147], v[96:111]
	v_cvt_pk_bf16_f32 v125, v243, v244
	v_cvt_pk_bf16_f32 v126, v245, v246
	v_cvt_pk_bf16_f32 v127, v247, v248
	v_cvt_pk_bf16_f32 v112, v112, v113
	v_cvt_pk_bf16_f32 v113, v114, v115
	v_cvt_pk_bf16_f32 v114, v116, v117
	v_cvt_pk_bf16_f32 v115, v118, v119
	v_cvt_pk_bf16_f32 v116, v168, v169
	v_cvt_pk_bf16_f32 v117, v170, v171
	v_cvt_pk_bf16_f32 v118, v172, v173
	v_cvt_pk_bf16_f32 v119, v174, v175
	s_add_u32 s24, s34, 0x2380c000
	s_addc_u32 s25, s35, 0
	s_add_u32 s34, s34, 0x2380e000
	s_addc_u32 s35, s35, 0
	s_add_u32 s66, s37, 0x21886000
	s_addc_u32 s67, s64, 0
	global_load_dwordx4 v[176:179], v200, s[24:25]
	global_load_dwordx4 v[172:175], v200, s[34:35]
	s_nop 0
	global_load_dwordx4 v[168:171], v201, s[66:67]
	s_and_b64 vcc, exec, s[2:3]
	s_cbranch_vccnz .LBB4_798
	s_mov_b64 s[2:3], s[8:9]
	global_store_dwordx2 v193, v[184:185], s[2:3] nt

; DI void pv_all_sm(f32x16* o, int vb, bf16x8 pa0, bf16x8 pa1, bf16x8 pa2, bf16x8 pa3, f32x16& p0, f32x16& p1, float& m_ref, f32x16& negm, float& alpha) {
;     ...
;     pv_one<3>(o[3], vb, pa0, pa1, pa2, pa3);
; #pragma unroll
;     for (int r = 0; r < 16; ++r) p0[r] = __builtin_amdgcn_exp2f(p0[r]);
; DI void attn_pass(const Frame& F, CvRide& cv, const bf16_t* __restrict__ Qb, const bf16_t* __restrict__ Kh, const bf16_t* __restrict__ Vh, char* lds, f32x16 (&o)[4], float& l_out, const int wave_s) {
;     ...
;     for (int j = 1; j + 2 < NT; j += 2) {
;         AT_STEP(pB0, pB1, pA0, pA1, alB, alA, j, true);
;         AT_STEP(pA0, pA1, pB0, pB1, alA, alB, j + 1, true);
;     }
.LBB4_806:
	s_add_u32 s18, s18, 0x4000
	v_exp_f32_e32 v220, v128
	v_exp_f32_e32 v222, v129
	v_exp_f32_e32 v179, v130
	v_exp_f32_e32 v221, v131
	v_exp_f32_e32 v177, v132
	v_exp_f32_e32 v219, v133
	v_exp_f32_e32 v176, v134
	v_exp_f32_e32 v178, v135
	v_exp_f32_e32 v173, v136
	v_exp_f32_e32 v175, v137
	v_exp_f32_e32 v171, v138
	v_exp_f32_e32 v174, v139
	v_exp_f32_e32 v169, v140
	v_exp_f32_e32 v172, v141
	v_exp_f32_e32 v168, v142
	v_exp_f32_e32 v170, v143
	s_addc_u32 s19, s19, 0
	s_add_u32 s16, s16, 0x8000
	v_fma_f32 v112, v211, v183, v215
	s_addc_u32 s17, s17, 0
	s_add_i32 s27, s27, 2
	v_fma_f32 v183, v112, v180, v217
	s_cmp_gt_u32 s27, 61
	s_waitcnt lgkmcnt(0)
	s_barrier
	s_cbranch_scc1 .LBB4_812
	s_mov_b32 s22, s15
	s_mov_b32 s15, s30
	v_mov_b32_e32 v211, v182
	s_branch .LBB4_765

; #define AT_SBAR() __builtin_amdgcn_sched_barrier(0)
; #define AT_CV_READ() do { if (cv.pend) { const char* t_ = lds + cv_lr + ((cv.ci - 1) & 1) * CV_TILE; cvr0 = *(const unsigned*)t_; cvr1 = *(const unsigned*)(t_ + 4); } } while (0)
; #define AT_CV_STORE() do { if (cv.pend) { GAS unsigned char* gd_ = (GAS unsigned char*)cv.sdst; unsigned o_ = cv_sto; asm volatile("" : "+s"(gd_), "+v"(o_)); __builtin_nontemporal_store((u32x2){cvr0, cvr1}, (GAS u32x2*)(gd_ + (size_t)o_)); cv.pend = 0; } } while (0)
; DI void attn_pass(const Frame& F, CvRide& cv, const bf16_t* __restrict__ Qb, const bf16_t* __restrict__ Kh, const bf16_t* __restrict__ Vh, char* lds, f32x16 (&o)[4], float& l_out, const int wave_s) {
;     ...
;     AT_STEP(pB0, pB1, pA0, pA1, alB, alA, NT - 1, false);
;     AT_CV_READ(); AT_CV_STORE();
;     finishSM(pB0, pB1, alB, l_reg, pa0, pa1, pa2, pa3); AT_SBAR();
.LBB4_812:
	v_mov_b32_e32 v254, v183
	s_nop 1
	v_permlane32_swap_b32_e32 v183, v254
	v_add_f32_e32 v183, v183, v254
	v_mov_b64_e32 v[64:65], v[80:81]
	v_mov_b64_e32 v[66:67], v[82:83]
	v_mov_b64_e32 v[68:69], v[84:85]
	v_mov_b64_e32 v[70:71], v[86:87]
	v_mov_b64_e32 v[72:73], v[88:89]
	v_mov_b64_e32 v[74:75], v[90:91]
	v_mov_b64_e32 v[76:77], v[92:93]
	v_mov_b64_e32 v[78:79], v[94:95]
	s_and_b64 vcc, exec, s[22:23]
	s_cbranch_vccz .LBB4_814
	s_andn2_b32 s15, 1, s58
	s_mulk_i32 s15, 0x1100
	v_add_u32_e32 v80, s15, v194
	ds_read2_b32 v[184:185], v80 offset1:1

; DI void finishSM(f32x16& p0, f32x16& p1, float alpha, float& l_reg, bf16x8& pa0, bf16x8& pa1, bf16x8& pa2, bf16x8& pa3) {
; #pragma unroll
;     for (int r = 0; r < 16; ++r) p1[r] = __builtin_amdgcn_exp2f(p1[r]);
;     float ps = 0;
; #pragma unroll
;     for (int r = 0; r < 16; ++r) ps += p0[r];
; #pragma unroll
;     for (int r = 0; r < 16; ++r) ps += p1[r];
;     { auto rr = __builtin_amdgcn_permlane32_swap(__float_as_uint(ps), __float_as_uint(ps), false, false); ps = __uint_as_float(rr[0]) + __uint_as_float(rr[1]); }
;     l_reg = l_reg * alpha + ps;
;     ...
;     AT_PK4(p0, 0, pa0); AT_PK4(p0, 8, pa1); AT_PK4(p1, 0, pa2); AT_PK4(p1, 8, pa3);
;     ...
; }
; DI void qkt(f32x16& p0, f32x16& p1, const char* Ks, const bf16x8* qr, const f32x16& negm, int r32, int hi) {
; #pragma unroll
;     for (int d0 = 0; d0 < 4; ++d0) { const int cb = (d0 * 16 + hi * 8) * 2;
;         const bf16x8 b0 = *reinterpret_cast<const bf16x8*>(Ks + AT_KSWZ(r32, cb));
;         const bf16x8 b1 = *reinterpret_cast<const bf16x8*>(Ks + AT_KSWZ(32 + r32, cb));
;         p0 = __builtin_amdgcn_mfma_f32_32x32x16_bf16(b0, qr[d0], d0 == 0 ? negm : p0, 0, 0, 0);
;         p1 = __builtin_amdgcn_mfma_f32_32x32x16_bf16(b1, qr[d0], d0 == 0 ? negm : p1, 0, 0, 0); }
.LBB4_849:
	s_lshl_b32 s26, s64, 13
	s_add_i32 s26, s26, 0
	v_add_u32_e32 v72, s26, v204
	v_add_u32_e32 v112, s26, v205
	v_add_u32_e32 v180, s26, v206
	s_waitcnt lgkmcnt(1)
	v_mfma_f32_32x32x16_bf16 v[128:143], v[64:67], v[156:159], v[80:95]
	ds_read_b128 v[64:67], v72 offset:49152
	ds_read_b128 v[72:75], v72 offset:53248
	ds_read_b128 v[76:79], v112 offset:49152
	ds_read_b128 v[220:223], v112 offset:53248
	v_exp_f32_e32 v182, v97
	v_exp_f32_e32 v213, v98
	v_exp_f32_e32 v214, v99
	v_exp_f32_e32 v219, v100
	v_exp_f32_e32 v228, v101
	s_waitcnt lgkmcnt(4)
	v_mfma_f32_32x32x16_bf16 v[112:127], v[68:71], v[156:159], v[80:95]
	ds_read_b128 v[68:71], v180 offset:49152
	ds_read_b128 v[224:227], v180 offset:53248
	v_exp_f32_e32 v180, v96
	v_cvt_pk_bf16_f32 v96, v216, v218
	v_cvt_pk_bf16_f32 v97, v179, v217
	v_cvt_pk_bf16_f32 v98, v177, v215
	v_cvt_pk_bf16_f32 v99, v176, v178
	s_waitcnt lgkmcnt(4)
	v_mfma_f32_32x32x16_bf16 v[112:127], v[72:75], v[152:155], v[112:127]
	v_add_f32_e32 v75, 0, v216
	v_add_f32_e32 v75, v218, v75
	v_add_f32_e32 v75, v179, v75
	v_add_f32_e32 v75, v217, v75
	v_add_f32_e32 v75, v177, v75
	v_add_f32_e32 v75, v215, v75
	v_add_f32_e32 v75, v176, v75
	v_mfma_f32_32x32x16_bf16 v[128:143], v[64:67], v[152:155], v[128:143]
	v_add_f32_e32 v75, v178, v75
	v_add_f32_e32 v75, v173, v75
	v_add_f32_e32 v75, v175, v75
	v_add_f32_e32 v75, v171, v75
	v_add_f32_e32 v75, v174, v75
	v_add_f32_e32 v75, v169, v75
	v_add_f32_e32 v75, v172, v75
	s_waitcnt lgkmcnt(3)
	v_mfma_f32_32x32x16_bf16 v[128:143], v[76:79], v[148:151], v[128:143]
	v_add_f32_e32 v75, v168, v75
	v_add_f32_e32 v75, v170, v75
	v_add_f32_e32 v75, v180, v75
	v_add_f32_e32 v75, v182, v75
	v_exp_f32_e32 v64, v102
	v_exp_f32_e32 v65, v103
	v_exp_f32_e32 v66, v104
	s_waitcnt lgkmcnt(2)
	v_mfma_f32_32x32x16_bf16 v[112:127], v[220:223], v[148:151], v[112:127]
	v_exp_f32_e32 v67, v105
	v_exp_f32_e32 v105, v106
	v_exp_f32_e32 v106, v107
	v_exp_f32_e32 v107, v108
	v_exp_f32_e32 v72, v109
	v_exp_f32_e32 v73, v110
	v_exp_f32_e32 v74, v111
	s_waitcnt lgkmcnt(1)
	v_mfma_f32_32x32x16_bf16 v[128:143], v[68:71], v[144:147], v[128:143]
	v_add_f32_e32 v68, v213, v75
	v_add_f32_e32 v68, v214, v68
	v_add_f32_e32 v68, v219, v68
	v_add_f32_e32 v68, v228, v68
	v_add_f32_e32 v68, v64, v68
	v_add_f32_e32 v68, v65, v68
	v_add_f32_e32 v68, v66, v68
	v_add_f32_e32 v68, v67, v68
	s_waitcnt lgkmcnt(0)
	v_mfma_f32_32x32x16_bf16 v[112:127], v[224:227], v[144:147], v[112:127]
	v_add_f32_e32 v68, v105, v68
	v_add_f32_e32 v68, v106, v68
	v_add_f32_e32 v68, v107, v68
	v_add_f32_e32 v68, v72, v68
	v_add_f32_e32 v68, v73, v68
	v_add_f32_e32 v211, v74, v68
	v_cvt_pk_bf16_f32 v108, v173, v175
	v_cvt_pk_bf16_f32 v109, v171, v174
	v_cvt_pk_bf16_f32 v110, v169, v172
	v_cvt_pk_bf16_f32 v111, v168, v170
	v_cvt_pk_bf16_f32 v100, v180, v182
	v_cvt_pk_bf16_f32 v101, v213, v214
	v_cvt_pk_bf16_f32 v102, v219, v228
	v_cvt_pk_bf16_f32 v103, v64, v65
	v_cvt_pk_bf16_f32 v104, v66, v67
	v_cvt_pk_bf16_f32 v105, v105, v106
	v_cvt_pk_bf16_f32 v106, v107, v72
	v_cvt_pk_bf16_f32 v107, v73, v74
	s_add_u32 s66, s46, s28
	s_addc_u32 s67, s47, s29
	s_add_u32 s34, s66, 0x23808000
	s_addc_u32 s35, s67, 0
	s_add_u32 s76, s66, 0x2380a000
	s_addc_u32 s77, s67, 0
	s_add_u32 s74, s46, s24
	s_addc_u32 s75, s47, s25
	s_add_u32 s78, s74, 0x21804000
	s_addc_u32 s79, s75, 0
	global_load_dwordx4 v[176:179], v196, s[34:35]
	global_load_dwordx4 v[172:175], v196, s[76:77]
	global_load_dwordx4 v[168:171], v197, s[78:79]
	s_andn2_b64 vcc, exec, s[2:3]
	s_cbranch_vccnz .LBB4_851
	s_mov_b64 s[2:3], s[8:9]
	global_store_dwordx2 v188, v[184:185], s[2:3] nt

; DI void finishSM(f32x16& p0, f32x16& p1, float alpha, float& l_reg, bf16x8& pa0, bf16x8& pa1, bf16x8& pa2, bf16x8& pa3) {
; #pragma unroll
;     for (int r = 0; r < 16; ++r) p1[r] = __builtin_amdgcn_exp2f(p1[r]);
;     float ps = 0;
; #pragma unroll
;     for (int r = 0; r < 16; ++r) ps += p0[r];
; #pragma unroll
;     for (int r = 0; r < 16; ++r) ps += p1[r];
;     { auto rr = __builtin_amdgcn_permlane32_swap(__float_as_uint(ps), __float_as_uint(ps), false, false); ps = __uint_as_float(rr[0]) + __uint_as_float(rr[1]); }
;     l_reg = l_reg * alpha + ps;
;     ...
;     AT_PK4(p0, 0, pa0); AT_PK4(p0, 8, pa1); AT_PK4(p1, 0, pa2); AT_PK4(p1, 8, pa3);
;     ...
; }
; DI void qkt(f32x16& p0, f32x16& p1, const char* Ks, const bf16x8* qr, const f32x16& negm, int r32, int hi) {
; #pragma unroll
;     for (int d0 = 0; d0 < 4; ++d0) { const int cb = (d0 * 16 + hi * 8) * 2;
;         const bf16x8 b0 = *reinterpret_cast<const bf16x8*>(Ks + AT_KSWZ(r32, cb));
;         const bf16x8 b1 = *reinterpret_cast<const bf16x8*>(Ks + AT_KSWZ(32 + r32, cb));
;         p0 = __builtin_amdgcn_mfma_f32_32x32x16_bf16(b0, qr[d0], d0 == 0 ? negm : p0, 0, 0, 0);
;         p1 = __builtin_amdgcn_mfma_f32_32x32x16_bf16(b1, qr[d0], d0 == 0 ? negm : p1, 0, 0, 0); }
.LBB4_870:
	v_exp_f32_e32 v182, v128
	v_exp_f32_e32 v230, v129
	v_exp_f32_e32 v231, v130
	v_exp_f32_e32 v232, v131
	v_exp_f32_e32 v233, v132
	v_exp_f32_e32 v234, v133
	v_exp_f32_e32 v235, v134
	v_exp_f32_e32 v236, v135
	v_exp_f32_e32 v237, v136
	v_exp_f32_e32 v238, v137
	v_exp_f32_e32 v239, v138
	v_exp_f32_e32 v240, v139
	v_exp_f32_e32 v241, v140
	v_exp_f32_e32 v242, v141
	v_exp_f32_e32 v243, v142
	v_exp_f32_e32 v244, v143
	v_add_u32_e32 v101, s76, v204
	v_add_u32_e32 v102, s76, v205
	v_add_u32_e32 v103, s76, v206
	ds_read_b128 v[172:175], v101 offset:49152
	ds_read_b128 v[176:179], v101 offset:53248
	ds_read_b128 v[214:217], v102 offset:49152
	ds_read_b128 v[218:221], v102 offset:53248
	ds_read_b128 v[222:225], v103 offset:49152
	ds_read_b128 v[226:229], v103 offset:53248
	v_exp_f32_e32 v112, v112
	v_exp_f32_e32 v113, v113
	v_exp_f32_e32 v114, v114
	s_waitcnt lgkmcnt(7)
	v_mfma_f32_32x32x16_bf16 v[128:143], v[96:99], v[156:159], v[80:95]
	v_exp_f32_e32 v115, v115
	v_exp_f32_e32 v116, v116
	v_exp_f32_e32 v117, v117
	v_exp_f32_e32 v118, v118
	v_exp_f32_e32 v119, v119
	s_waitcnt lgkmcnt(6)
	v_mfma_f32_32x32x16_bf16 v[96:111], v[168:171], v[156:159], v[80:95]
	v_exp_f32_e32 v168, v120
	v_add_f32_e32 v120, 0, v182
	v_add_f32_e32 v120, v230, v120
	v_add_f32_e32 v120, v231, v120
	v_add_f32_e32 v120, v232, v120
	v_add_f32_e32 v120, v233, v120
	v_add_f32_e32 v120, v234, v120
	v_add_f32_e32 v120, v235, v120
	v_add_f32_e32 v120, v236, v120
	v_add_f32_e32 v120, v237, v120
	v_add_f32_e32 v120, v238, v120
	s_waitcnt lgkmcnt(5)
	v_mfma_f32_32x32x16_bf16 v[128:143], v[172:175], v[152:155], v[128:143]
	v_add_f32_e32 v120, v239, v120
	v_add_f32_e32 v120, v240, v120
	v_add_f32_e32 v120, v241, v120
	v_add_f32_e32 v120, v242, v120
	v_add_f32_e32 v120, v243, v120
	v_add_f32_e32 v120, v244, v120
	v_add_f32_e32 v120, v112, v120
	s_waitcnt lgkmcnt(4)
	v_mfma_f32_32x32x16_bf16 v[96:111], v[176:179], v[152:155], v[96:111]
	v_add_f32_e32 v120, v113, v120
	v_add_f32_e32 v120, v114, v120
	v_add_f32_e32 v120, v115, v120
	v_add_f32_e32 v120, v116, v120
	v_exp_f32_e32 v169, v121
	v_add_f32_e32 v120, v117, v120
	v_exp_f32_e32 v170, v122
	s_waitcnt lgkmcnt(3)
	v_mfma_f32_32x32x16_bf16 v[128:143], v[214:217], v[148:151], v[128:143]
	v_add_f32_e32 v120, v118, v120
	v_exp_f32_e32 v171, v123
	v_add_f32_e32 v120, v119, v120
	v_exp_f32_e32 v172, v124
	v_add_f32_e32 v120, v168, v120
	v_exp_f32_e32 v173, v125
	v_add_f32_e32 v120, v169, v120
	s_waitcnt lgkmcnt(2)
	v_mfma_f32_32x32x16_bf16 v[96:111], v[218:221], v[148:151], v[96:111]
	v_exp_f32_e32 v174, v126
	v_add_f32_e32 v120, v170, v120
	v_exp_f32_e32 v175, v127
	v_add_f32_e32 v120, v171, v120
	v_add_f32_e32 v120, v172, v120
	v_add_f32_e32 v120, v173, v120
	v_add_f32_e32 v120, v174, v120
	s_waitcnt lgkmcnt(1)
	v_mfma_f32_32x32x16_bf16 v[128:143], v[222:225], v[144:147], v[128:143]
	v_add_f32_e32 v213, v175, v120
	v_cvt_pk_bf16_f32 v120, v182, v230
	v_cvt_pk_bf16_f32 v121, v231, v232
	v_cvt_pk_bf16_f32 v122, v233, v234
	v_cvt_pk_bf16_f32 v123, v235, v236
	v_cvt_pk_bf16_f32 v124, v237, v238
	s_waitcnt lgkmcnt(0)
	v_mfma_f32_32x32x16_bf16 v[96:111], v[226:229], v[144:147], v[96:111]
	v_cvt_pk_bf16_f32 v125, v239, v240
	v_cvt_pk_bf16_f32 v126, v241, v242
	v_cvt_pk_bf16_f32 v127, v243, v244
	v_cvt_pk_bf16_f32 v112, v112, v113
	v_cvt_pk_bf16_f32 v113, v114, v115
	v_cvt_pk_bf16_f32 v114, v116, v117
	v_cvt_pk_bf16_f32 v115, v118, v119
	v_cvt_pk_bf16_f32 v116, v168, v169
	v_cvt_pk_bf16_f32 v117, v170, v171
	v_cvt_pk_bf16_f32 v118, v172, v173
	v_cvt_pk_bf16_f32 v119, v174, v175
	s_add_u32 s34, s66, 0x2380c000
	s_addc_u32 s35, s67, 0
	s_add_u32 s66, s66, 0x2380e000
	s_addc_u32 s67, s67, 0
	s_add_u32 s74, s74, 0x21806000
	s_addc_u32 s75, s75, 0
	global_load_dwordx4 v[176:179], v196, s[34:35]
	global_load_dwordx4 v[172:175], v196, s[66:67]
	s_nop 0
	global_load_dwordx4 v[168:171], v197, s[74:75]
	s_and_b64 vcc, exec, s[2:3]
	s_cbranch_vccnz .LBB4_872
	s_mov_b64 s[2:3], s[8:9]
	global_store_dwordx2 v188, v[184:185], s[2:3] nt

; DI void pv_all_sm(f32x16* o, int vb, bf16x8 pa0, bf16x8 pa1, bf16x8 pa2, bf16x8 pa3, f32x16& p0, f32x16& p1, float& m_ref, f32x16& negm, float& alpha) {
;     ...
;     pv_one<3>(o[3], vb, pa0, pa1, pa2, pa3);
; #pragma unroll
;     for (int r = 0; r < 16; ++r) p0[r] = __builtin_amdgcn_exp2f(p0[r]);
; DI void attn_pass(const Frame& F, CvRide& cv, const bf16_t* __restrict__ Qb, const bf16_t* __restrict__ Kh, const bf16_t* __restrict__ Vh, char* lds, f32x16 (&o)[4], float& l_out, const int wave_s) {
;     ...
;     for (int j = 1; j + 2 < NT; j += 2) {
;         AT_STEP(pB0, pB1, pA0, pA1, alB, alA, j, true);
;         AT_STEP(pA0, pA1, pB0, pB1, alA, alB, j + 1, true);
;     }
.LBB4_880:
	s_add_u32 s24, s24, 0x4000
	v_exp_f32_e32 v216, v128
	v_exp_f32_e32 v218, v129
	v_exp_f32_e32 v179, v130
	v_exp_f32_e32 v217, v131
	v_exp_f32_e32 v177, v132
	v_exp_f32_e32 v215, v133
	v_exp_f32_e32 v176, v134
	v_exp_f32_e32 v178, v135
	v_exp_f32_e32 v173, v136
	v_exp_f32_e32 v175, v137
	v_exp_f32_e32 v171, v138
	v_exp_f32_e32 v174, v139
	v_exp_f32_e32 v169, v140
	v_exp_f32_e32 v172, v141
	v_exp_f32_e32 v168, v142
	v_exp_f32_e32 v170, v143
	s_addc_u32 s25, s25, 0
	s_add_u32 s28, s28, 0x8000
	v_fma_f32 v112, v207, v183, v211
	s_addc_u32 s29, s29, 0
	s_add_i32 s23, s23, 2
	v_fma_f32 v183, v112, v180, v213
	s_cmp_gt_u32 s23, 61
	s_waitcnt lgkmcnt(0)
	s_barrier
	s_cbranch_scc1 .LBB4_886
	s_mov_b32 s30, s57
	s_mov_b32 s57, s64
	v_mov_b32_e32 v207, v182
	s_branch .LBB4_839

; #define AT_SBAR() __builtin_amdgcn_sched_barrier(0)
; #define AT_CV_READ() do { if (cv.pend) { const char* t_ = lds + cv_lr + ((cv.ci - 1) & 1) * CV_TILE; cvr0 = *(const unsigned*)t_; cvr1 = *(const unsigned*)(t_ + 4); } } while (0)
; #define AT_CV_STORE() do { if (cv.pend) { GAS unsigned char* gd_ = (GAS unsigned char*)cv.sdst; unsigned o_ = cv_sto; asm volatile("" : "+s"(gd_), "+v"(o_)); __builtin_nontemporal_store((u32x2){cvr0, cvr1}, (GAS u32x2*)(gd_ + (size_t)o_)); cv.pend = 0; } } while (0)
; DI void attn_pass(const Frame& F, CvRide& cv, const bf16_t* __restrict__ Qb, const bf16_t* __restrict__ Kh, const bf16_t* __restrict__ Vh, char* lds, f32x16 (&o)[4], float& l_out, const int wave_s) {
;     ...
;     AT_STEP(pB0, pB1, pA0, pA1, alB, alA, NT - 1, false);
;     AT_CV_READ(); AT_CV_STORE();
;     finishSM(pB0, pB1, alB, l_reg, pa0, pa1, pa2, pa3); AT_SBAR();
.LBB4_886:
	v_mov_b32_e32 v254, v183
	s_nop 1
	v_permlane32_swap_b32_e32 v183, v254
	v_add_f32_e32 v183, v183, v254
	v_mov_b64_e32 v[64:65], v[80:81]
	v_mov_b64_e32 v[66:67], v[82:83]
	v_mov_b64_e32 v[68:69], v[84:85]
	v_mov_b64_e32 v[70:71], v[86:87]
	v_mov_b64_e32 v[72:73], v[88:89]
	v_mov_b64_e32 v[74:75], v[90:91]
	v_mov_b64_e32 v[76:77], v[92:93]
	v_mov_b64_e32 v[78:79], v[94:95]
	s_and_b64 vcc, exec, s[30:31]
	s_cbranch_vccz .LBB4_888
	s_andn2_b32 s15, 1, s58
	s_mulk_i32 s15, 0x1100
	v_add_u32_e32 v80, s15, v189
	ds_read2_b32 v[184:185], v80 offset1:1

; DI void finishSM(f32x16& p0, f32x16& p1, float alpha, float& l_reg, bf16x8& pa0, bf16x8& pa1, bf16x8& pa2, bf16x8& pa3) {
; #pragma unroll
;     for (int r = 0; r < 16; ++r) p1[r] = __builtin_amdgcn_exp2f(p1[r]);
;     float ps = 0;
; #pragma unroll
;     for (int r = 0; r < 16; ++r) ps += p0[r];
; #pragma unroll
;     for (int r = 0; r < 16; ++r) ps += p1[r];
;     { auto rr = __builtin_amdgcn_permlane32_swap(__float_as_uint(ps), __float_as_uint(ps), false, false); ps = __uint_as_float(rr[0]) + __uint_as_float(rr[1]); }
;     l_reg = l_reg * alpha + ps;
;     ...
;     AT_PK4(p0, 0, pa0); AT_PK4(p0, 8, pa1); AT_PK4(p1, 0, pa2); AT_PK4(p1, 8, pa3);
;     ...
; }
; DI void qkt(f32x16& p0, f32x16& p1, const char* Ks, const bf16x8* qr, const f32x16& negm, int r32, int hi) {
; #pragma unroll
;     for (int d0 = 0; d0 < 4; ++d0) { const int cb = (d0 * 16 + hi * 8) * 2;
;         const bf16x8 b0 = *reinterpret_cast<const bf16x8*>(Ks + AT_KSWZ(r32, cb));
;         const bf16x8 b1 = *reinterpret_cast<const bf16x8*>(Ks + AT_KSWZ(32 + r32, cb));
;         p0 = __builtin_amdgcn_mfma_f32_32x32x16_bf16(b0, qr[d0], d0 == 0 ? negm : p0, 0, 0, 0);
;         p1 = __builtin_amdgcn_mfma_f32_32x32x16_bf16(b1, qr[d0], d0 == 0 ? negm : p1, 0, 0, 0); }
.LBB4_923:
	s_lshl_b32 s18, s30, 13
	s_add_i32 s18, s18, 0
	v_add_u32_e32 v72, s18, v208
	v_add_u32_e32 v112, s18, v209
	v_add_u32_e32 v180, s18, v210
	s_waitcnt lgkmcnt(1)
	v_mfma_f32_32x32x16_bf16 v[128:143], v[64:67], v[156:159], v[80:95]
	ds_read_b128 v[64:67], v72 offset:49152
	ds_read_b128 v[72:75], v72 offset:53248
	ds_read_b128 v[76:79], v112 offset:49152
	ds_read_b128 v[224:227], v112 offset:53248
	v_exp_f32_e32 v182, v97
	v_exp_f32_e32 v217, v98
	v_exp_f32_e32 v218, v99
	v_exp_f32_e32 v223, v100
	v_exp_f32_e32 v232, v101
	s_waitcnt lgkmcnt(4)
	v_mfma_f32_32x32x16_bf16 v[112:127], v[68:71], v[156:159], v[80:95]
	ds_read_b128 v[68:71], v180 offset:49152
	ds_read_b128 v[228:231], v180 offset:53248
	v_exp_f32_e32 v180, v96
	v_cvt_pk_bf16_f32 v96, v220, v222
	v_cvt_pk_bf16_f32 v97, v179, v221
	v_cvt_pk_bf16_f32 v98, v177, v219
	v_cvt_pk_bf16_f32 v99, v176, v178
	s_waitcnt lgkmcnt(4)
	v_mfma_f32_32x32x16_bf16 v[112:127], v[72:75], v[152:155], v[112:127]
	v_add_f32_e32 v75, 0, v220
	v_add_f32_e32 v75, v222, v75
	v_add_f32_e32 v75, v179, v75
	v_add_f32_e32 v75, v221, v75
	v_add_f32_e32 v75, v177, v75
	v_add_f32_e32 v75, v219, v75
	v_add_f32_e32 v75, v176, v75
	v_mfma_f32_32x32x16_bf16 v[128:143], v[64:67], v[152:155], v[128:143]
	v_add_f32_e32 v75, v178, v75
	v_add_f32_e32 v75, v173, v75
	v_add_f32_e32 v75, v175, v75
	v_add_f32_e32 v75, v171, v75
	v_add_f32_e32 v75, v174, v75
	v_add_f32_e32 v75, v169, v75
	v_add_f32_e32 v75, v172, v75
	s_waitcnt lgkmcnt(3)
	v_mfma_f32_32x32x16_bf16 v[128:143], v[76:79], v[148:151], v[128:143]
	v_add_f32_e32 v75, v168, v75
	v_add_f32_e32 v75, v170, v75
	v_add_f32_e32 v75, v180, v75
	v_add_f32_e32 v75, v182, v75
	v_exp_f32_e32 v64, v102
	v_exp_f32_e32 v65, v103
	v_exp_f32_e32 v66, v104
	s_waitcnt lgkmcnt(2)
	v_mfma_f32_32x32x16_bf16 v[112:127], v[224:227], v[148:151], v[112:127]
	v_exp_f32_e32 v67, v105
	v_exp_f32_e32 v105, v106
	v_exp_f32_e32 v106, v107
	v_exp_f32_e32 v107, v108
	v_exp_f32_e32 v72, v109
	v_exp_f32_e32 v73, v110
	v_exp_f32_e32 v74, v111
	s_waitcnt lgkmcnt(1)
	v_mfma_f32_32x32x16_bf16 v[128:143], v[68:71], v[144:147], v[128:143]
	v_add_f32_e32 v68, v217, v75
	v_add_f32_e32 v68, v218, v68
	v_add_f32_e32 v68, v223, v68
	v_add_f32_e32 v68, v232, v68
	v_add_f32_e32 v68, v64, v68
	v_add_f32_e32 v68, v65, v68
	v_add_f32_e32 v68, v66, v68
	v_add_f32_e32 v68, v67, v68
	s_waitcnt lgkmcnt(0)
	v_mfma_f32_32x32x16_bf16 v[112:127], v[228:231], v[144:147], v[112:127]
	v_add_f32_e32 v68, v105, v68
	v_add_f32_e32 v68, v106, v68
	v_add_f32_e32 v68, v107, v68
	v_add_f32_e32 v68, v72, v68
	v_add_f32_e32 v68, v73, v68
	v_add_f32_e32 v215, v74, v68
	v_cvt_pk_bf16_f32 v108, v173, v175
	v_cvt_pk_bf16_f32 v109, v171, v174
	v_cvt_pk_bf16_f32 v110, v169, v172
	v_cvt_pk_bf16_f32 v111, v168, v170
	v_cvt_pk_bf16_f32 v100, v180, v182
	v_cvt_pk_bf16_f32 v101, v217, v218
	v_cvt_pk_bf16_f32 v102, v223, v232
	v_cvt_pk_bf16_f32 v103, v64, v65
	v_cvt_pk_bf16_f32 v104, v66, v67
	v_cvt_pk_bf16_f32 v105, v105, v106
	v_cvt_pk_bf16_f32 v106, v107, v72
	v_cvt_pk_bf16_f32 v107, v73, v74
	s_add_u32 s34, s46, s16
	s_addc_u32 s35, s47, s17
	s_add_u32 s24, s34, 0x23808000
	s_addc_u32 s25, s35, 0
	s_add_u32 s54, s34, 0x2380a000
	s_addc_u32 s55, s35, 0
	s_add_u32 s42, s46, s20
	s_addc_u32 s43, s47, s21
	s_add_u32 s56, s42, 0x21884000
	s_addc_u32 s57, s43, 0
	global_load_dwordx4 v[176:179], v200, s[24:25]
	global_load_dwordx4 v[172:175], v200, s[54:55]
	global_load_dwordx4 v[168:171], v201, s[56:57]
	s_andn2_b64 vcc, exec, s[2:3]
	s_cbranch_vccnz .LBB4_925
	s_mov_b64 s[2:3], s[8:9]
	global_store_dwordx2 v193, v[184:185], s[2:3] nt

; DI void finishSM(f32x16& p0, f32x16& p1, float alpha, float& l_reg, bf16x8& pa0, bf16x8& pa1, bf16x8& pa2, bf16x8& pa3) {
; #pragma unroll
;     for (int r = 0; r < 16; ++r) p1[r] = __builtin_amdgcn_exp2f(p1[r]);
;     float ps = 0;
; #pragma unroll
;     for (int r = 0; r < 16; ++r) ps += p0[r];
; #pragma unroll
;     for (int r = 0; r < 16; ++r) ps += p1[r];
;     { auto rr = __builtin_amdgcn_permlane32_swap(__float_as_uint(ps), __float_as_uint(ps), false, false); ps = __uint_as_float(rr[0]) + __uint_as_float(rr[1]); }
;     l_reg = l_reg * alpha + ps;
;     ...
;     AT_PK4(p0, 0, pa0); AT_PK4(p0, 8, pa1); AT_PK4(p1, 0, pa2); AT_PK4(p1, 8, pa3);
;     ...
; }
; DI void qkt(f32x16& p0, f32x16& p1, const char* Ks, const bf16x8* qr, const f32x16& negm, int r32, int hi) {
; #pragma unroll
;     for (int d0 = 0; d0 < 4; ++d0) { const int cb = (d0 * 16 + hi * 8) * 2;
;         const bf16x8 b0 = *reinterpret_cast<const bf16x8*>(Ks + AT_KSWZ(r32, cb));
;         const bf16x8 b1 = *reinterpret_cast<const bf16x8*>(Ks + AT_KSWZ(32 + r32, cb));
;         p0 = __builtin_amdgcn_mfma_f32_32x32x16_bf16(b0, qr[d0], d0 == 0 ? negm : p0, 0, 0, 0);
;         p1 = __builtin_amdgcn_mfma_f32_32x32x16_bf16(b1, qr[d0], d0 == 0 ? negm : p1, 0, 0, 0); }
; }
.LBB4_944:
	v_exp_f32_e32 v182, v128
	v_exp_f32_e32 v234, v129
	v_exp_f32_e32 v235, v130
	v_exp_f32_e32 v236, v131
	v_exp_f32_e32 v237, v132
	v_exp_f32_e32 v238, v133
	v_exp_f32_e32 v239, v134
	v_exp_f32_e32 v240, v135
	v_exp_f32_e32 v241, v136
	v_exp_f32_e32 v242, v137
	v_exp_f32_e32 v243, v138
	v_exp_f32_e32 v244, v139
	v_exp_f32_e32 v245, v140
	v_exp_f32_e32 v246, v141
	v_exp_f32_e32 v247, v142
	v_exp_f32_e32 v248, v143
	v_add_u32_e32 v101, s54, v208
	v_add_u32_e32 v102, s54, v209
	v_add_u32_e32 v103, s54, v210
	ds_read_b128 v[172:175], v101 offset:49152
	ds_read_b128 v[176:179], v101 offset:53248
	ds_read_b128 v[218:221], v102 offset:49152
	ds_read_b128 v[222:225], v102 offset:53248
	ds_read_b128 v[226:229], v103 offset:49152
	ds_read_b128 v[230:233], v103 offset:53248
	v_exp_f32_e32 v112, v112
	v_exp_f32_e32 v113, v113
	v_exp_f32_e32 v114, v114
	s_waitcnt lgkmcnt(7)
	v_mfma_f32_32x32x16_bf16 v[128:143], v[96:99], v[156:159], v[80:95]
	v_exp_f32_e32 v115, v115
	v_exp_f32_e32 v116, v116
	v_exp_f32_e32 v117, v117
	v_exp_f32_e32 v118, v118
	v_exp_f32_e32 v119, v119
	s_waitcnt lgkmcnt(6)
	v_mfma_f32_32x32x16_bf16 v[96:111], v[168:171], v[156:159], v[80:95]
	v_exp_f32_e32 v168, v120
	v_add_f32_e32 v120, 0, v182
	v_add_f32_e32 v120, v234, v120
	v_add_f32_e32 v120, v235, v120
	v_add_f32_e32 v120, v236, v120
	v_add_f32_e32 v120, v237, v120
	v_add_f32_e32 v120, v238, v120
	v_add_f32_e32 v120, v239, v120
	v_add_f32_e32 v120, v240, v120
	v_add_f32_e32 v120, v241, v120
	v_add_f32_e32 v120, v242, v120
	s_waitcnt lgkmcnt(5)
	v_mfma_f32_32x32x16_bf16 v[128:143], v[172:175], v[152:155], v[128:143]
	v_add_f32_e32 v120, v243, v120
	v_add_f32_e32 v120, v244, v120
	v_add_f32_e32 v120, v245, v120
	v_add_f32_e32 v120, v246, v120
	v_add_f32_e32 v120, v247, v120
	v_add_f32_e32 v120, v248, v120
	v_add_f32_e32 v120, v112, v120
	s_waitcnt lgkmcnt(4)
	v_mfma_f32_32x32x16_bf16 v[96:111], v[176:179], v[152:155], v[96:111]
	v_add_f32_e32 v120, v113, v120
	v_add_f32_e32 v120, v114, v120
	v_add_f32_e32 v120, v115, v120
	v_add_f32_e32 v120, v116, v120
	v_exp_f32_e32 v169, v121
	v_add_f32_e32 v120, v117, v120
	v_exp_f32_e32 v170, v122
	s_waitcnt lgkmcnt(3)
	v_mfma_f32_32x32x16_bf16 v[128:143], v[218:221], v[148:151], v[128:143]
	v_add_f32_e32 v120, v118, v120
	v_exp_f32_e32 v171, v123
	v_add_f32_e32 v120, v119, v120
	v_exp_f32_e32 v172, v124
	v_add_f32_e32 v120, v168, v120
	v_exp_f32_e32 v173, v125
	v_add_f32_e32 v120, v169, v120
	s_waitcnt lgkmcnt(2)
	v_mfma_f32_32x32x16_bf16 v[96:111], v[222:225], v[148:151], v[96:111]
	v_exp_f32_e32 v174, v126
	v_add_f32_e32 v120, v170, v120
	v_exp_f32_e32 v175, v127
	v_add_f32_e32 v120, v171, v120
	v_add_f32_e32 v120, v172, v120
	v_add_f32_e32 v120, v173, v120
	v_add_f32_e32 v120, v174, v120
	s_waitcnt lgkmcnt(1)
	v_mfma_f32_32x32x16_bf16 v[128:143], v[226:229], v[144:147], v[128:143]
	v_add_f32_e32 v217, v175, v120
	v_cvt_pk_bf16_f32 v120, v182, v234
	v_cvt_pk_bf16_f32 v121, v235, v236
	v_cvt_pk_bf16_f32 v122, v237, v238
	v_cvt_pk_bf16_f32 v123, v239, v240
	v_cvt_pk_bf16_f32 v124, v241, v242
	s_waitcnt lgkmcnt(0)
	v_mfma_f32_32x32x16_bf16 v[96:111], v[230:233], v[144:147], v[96:111]
	v_cvt_pk_bf16_f32 v125, v243, v244
	v_cvt_pk_bf16_f32 v126, v245, v246
	v_cvt_pk_bf16_f32 v127, v247, v248
	v_cvt_pk_bf16_f32 v112, v112, v113
	v_cvt_pk_bf16_f32 v113, v114, v115
	v_cvt_pk_bf16_f32 v114, v116, v117
	v_cvt_pk_bf16_f32 v115, v118, v119
	v_cvt_pk_bf16_f32 v116, v168, v169
	v_cvt_pk_bf16_f32 v117, v170, v171
	v_cvt_pk_bf16_f32 v118, v172, v173
	v_cvt_pk_bf16_f32 v119, v174, v175
	s_add_u32 s24, s34, 0x2380c000
	s_addc_u32 s25, s35, 0
	s_add_u32 s34, s34, 0x2380e000
	s_addc_u32 s35, s35, 0
	s_add_u32 s42, s42, 0x21886000
	s_addc_u32 s43, s43, 0
	global_load_dwordx4 v[176:179], v200, s[24:25]
	global_load_dwordx4 v[172:175], v200, s[34:35]
	s_nop 0
	global_load_dwordx4 v[168:171], v201, s[42:43]
	s_and_b64 vcc, exec, s[2:3]
	s_cbranch_vccnz .LBB4_946
	s_mov_b64 s[2:3], s[8:9]
	global_store_dwordx2 v193, v[184:185], s[2:3] nt

; DI void finishSM(f32x16& p0, f32x16& p1, float alpha, float& l_reg, bf16x8& pa0, bf16x8& pa1, bf16x8& pa2, bf16x8& pa3) {
;     ...
;     l_reg = l_reg * alpha + ps;
; DI void pv_all_sm(f32x16* o, int vb, bf16x8 pa0, bf16x8 pa1, bf16x8 pa2, bf16x8 pa3, f32x16& p0, f32x16& p1, float& m_ref, f32x16& negm, float& alpha) {
;     ...
;     pv_one<3>(o[3], vb, pa0, pa1, pa2, pa3);
; #pragma unroll
;     for (int r = 0; r < 16; ++r) p0[r] = __builtin_amdgcn_exp2f(p0[r]);
; }
.LBB4_954:
	s_add_u32 s20, s20, 0x4000
	v_exp_f32_e32 v220, v128
	v_exp_f32_e32 v222, v129
	v_exp_f32_e32 v179, v130
	v_exp_f32_e32 v221, v131
	v_exp_f32_e32 v177, v132
	v_exp_f32_e32 v219, v133
	v_exp_f32_e32 v176, v134
	v_exp_f32_e32 v178, v135
	v_exp_f32_e32 v173, v136
	v_exp_f32_e32 v175, v137
	v_exp_f32_e32 v171, v138
	v_exp_f32_e32 v174, v139
	v_exp_f32_e32 v169, v140
	v_exp_f32_e32 v172, v141
	v_exp_f32_e32 v168, v142
	v_exp_f32_e32 v170, v143
	s_addc_u32 s21, s21, 0
	s_add_u32 s16, s16, 0x8000
	v_fma_f32 v112, v211, v183, v215
	s_addc_u32 s17, s17, 0
	s_add_i32 s27, s27, 2
	v_fma_f32 v183, v112, v180, v217
	s_cmp_gt_u32 s27, 61
	s_waitcnt lgkmcnt(0)
	s_barrier
	s_cbranch_scc1 .LBB4_960
	s_mov_b32 s22, s15
	s_mov_b32 s15, s30
	v_mov_b32_e32 v211, v182
	s_branch .LBB4_913
